# speedup vs baseline: 1.0174x; 1.0174x over previous
_Z9l1_kernelPKiS0_P15HIP_vector_typeIjLj2EEPiS4_PKfS6_S6_S6_PfP6__half:
	s_cmp_gt_u32 s2, 42
	s_mov_b64 s[4:5], -1
	s_cbranch_scc0 .LBB0_17
	s_mul_i32 s15, s2, 0xeb
	s_add_i32 s3, s15, 0xffffd887
	s_min_i32 s16, s3, 0xc265
	s_add_i32 s12, s16, 0xeb
	s_cmp_ge_i32 s3, s12
	s_cbranch_scc1 .LBB0_16
	s_load_dwordx4 s[4:7], s[0:1], 0x28
	s_load_dwordx2 s[10:11], s[0:1], 0x38
	s_load_dwordx4 s[24:27], s[0:1], 0x40
	s_load_dwordx2 s[28:29], s[0:1], 0x50
	v_lshlrev_b32_e32 v1, 4, v0
	v_and_b32_e32 v2, 0x1f0, v1
	v_mov_b32_e32 v3, 0
	v_lshrrev_b32_e32 v1, 5, v0
	s_add_i32 s13, s16, 0xea
	s_waitcnt lgkmcnt(0)
	v_lshl_add_u64 v[110:111], s[4:5], 0, v[2:3]
	v_add_u32_e32 v2, s3, v1
	v_min_i32_e32 v2, s13, v2
	v_ashrrev_i32_e32 v3, 31, v2
	v_lshlrev_b64 v[2:3], 9, v[2:3]
	v_lshl_add_u64 v[10:11], v[110:111], 0, v[2:3]
	v_or_b32_e32 v2, 0x200, v0
	v_lshrrev_b32_e32 v146, 5, v2
	v_add_u32_e32 v2, s3, v146
	v_min_i32_e32 v2, s13, v2
	v_ashrrev_i32_e32 v3, 31, v2
	v_lshlrev_b64 v[2:3], 9, v[2:3]
	v_or_b32_e32 v147, 32, v1
	v_lshl_add_u64 v[12:13], v[110:111], 0, v[2:3]
	global_load_dwordx4 v[2:5], v[10:11], off nt
	global_load_dwordx4 v[6:9], v[12:13], off nt
	v_add_u32_e32 v10, s3, v147
	v_min_i32_e32 v10, s13, v10
	v_ashrrev_i32_e32 v11, 31, v10
	v_lshlrev_b64 v[10:11], 9, v[10:11]
	v_lshl_add_u64 v[10:11], v[110:111], 0, v[10:11]
	global_load_dwordx4 v[10:13], v[10:11], off nt
	v_lshrrev_b32_e32 v149, 6, v0
	s_movk_i32 s4, 0x200
	v_and_b32_e32 v150, 15, v0
	v_cmp_gt_u32_e32 vcc, s4, v0
	v_lshlrev_b32_e32 v151, 4, v149
	s_and_saveexec_b64 s[4:5], vcc
	s_xor_b64 s[4:5], exec, s[4:5]
	v_or_b32_e32 v32, v151, v150
	s_or_saveexec_b64 s[4:5], s[4:5]
	v_lshlrev_b32_e32 v14, 1, v150
	v_mov_b64_e32 v[30:31], s[6:7]
	s_xor_b64 exec, exec, s[4:5]
	v_and_b32_e32 v15, 0x60, v151
	v_bfe_u32 v16, v0, 6, 1
	v_or3_b32 v32, v16, v15, v14
	v_mov_b64_e32 v[30:31], s[10:11]
	s_or_b64 exec, exec, s[4:5]
	s_movk_i32 s17, 0x110
	s_mov_b32 s14, 0x7060302
	s_sub_i32 s19, s16, s3
	s_addk_i32 s19, 0x11a
	v_readfirstlane_b32 s30, v149
	v_bfe_u32 v152, v0, 4, 2
	v_lshlrev_b32_e32 v153, 5, v149
	v_and_b32_e32 v153, 0x60, v153
	v_or_b32_e32 v144, v151, v150
	v_lshlrev_b32_e32 v144, 2, v144
	v_lshl_add_u32 v144, v152, 12, v144
	v_lshlrev_b32_e32 v145, 3, v150
	v_lshl_add_u32 v145, v153, 2, v145
	v_lshl_add_u32 v145, v152, 12, v145
	s_waitcnt lgkmcnt(0)
	s_cmp_lt_u32 s30, 4
	s_cselect_b32 s20, s10, s24
	s_cselect_b32 s21, s11, s25
	s_add_u32 s32, s6, 0x4000
	s_addc_u32 s33, s7, 0
	s_add_u32 s34, s6, 0x8000
	s_addc_u32 s35, s7, 0
	s_add_u32 s36, s6, 0xc000
	s_addc_u32 s37, s7, 0
	s_add_u32 s38, s20, 0x4000
	s_addc_u32 s39, s21, 0
	s_add_u32 s40, s20, 0x8000
	s_addc_u32 s41, s21, 0
	s_add_u32 s42, s20, 0xc000
	s_addc_u32 s43, s21, 0
	s_mul_hi_u32 s5, s19, 0xaaaaaaab
	s_addk_i32 s16, 0xfa
	s_lshr_b32 s10, s5, 5
	s_mov_b32 s11, 0
	s_add_i32 s31, s30, s2
	s_and_b32 s31, s31, 7
	s_cmp_eq_u32 s31, 1
	s_cbranch_scc1 .Lw_rot_1
	s_cmp_eq_u32 s31, 2
	s_cbranch_scc1 .Lw_rot_2
	s_cmp_eq_u32 s31, 3
	s_cbranch_scc1 .Lw_rot_3
	s_cmp_eq_u32 s31, 4
	s_cbranch_scc1 .Lw_rot_4
	s_cmp_eq_u32 s31, 5
	s_cbranch_scc1 .Lw_rot_5
	s_cmp_eq_u32 s31, 6
	s_cbranch_scc1 .Lw_rot_6
	s_cmp_eq_u32 s31, 7
	s_cbranch_scc1 .Lw_rot_7

.LBB0_9:
	s_add_i32 s7, s11, 1
	s_cmp_lt_u32 s7, s10
	s_cselect_b64 s[4:5], -1, 0
	s_cmp_ge_u32 s7, s10
	s_cbranch_scc1 .LBB0_11
	s_mul_i32 s8, s7, 48
	s_add_i32 s8, s8, s3
	s_waitcnt vmcnt(2)
	v_add_u32_e32 v2, s8, v1
	v_min_i32_e32 v2, s13, v2
	v_ashrrev_i32_e32 v3, 31, v2
	v_lshlrev_b64 v[2:3], 9, v[2:3]
	s_waitcnt vmcnt(0)
	v_lshl_add_u64 v[10:11], v[110:111], 0, v[2:3]
	v_add_u32_e32 v2, s8, v146
	v_min_i32_e32 v2, s13, v2
	v_ashrrev_i32_e32 v3, 31, v2
	v_lshlrev_b64 v[2:3], 9, v[2:3]
	v_lshl_add_u64 v[12:13], v[110:111], 0, v[2:3]
	global_load_dwordx4 v[2:5], v[10:11], off nt
	global_load_dwordx4 v[6:9], v[12:13], off nt
	v_add_u32_e32 v10, s8, v147
	v_min_i32_e32 v10, s13, v10
	v_ashrrev_i32_e32 v11, 31, v10
	v_lshlrev_b64 v[10:11], 9, v[10:11]
	v_lshl_add_u64 v[10:11], v[110:111], 0, v[10:11]
	global_load_dwordx4 v[10:13], v[10:11], off nt
